# speedup vs baseline: 1.0382x; 1.0116x over previous
.LBB2_102:
	s_or_b64 exec, exec, s[0:1]
	v_lshl_or_b32 v232, s2, 9, v0
	v_lshlrev_b32_e32 v232, 4, v232
	global_load_dwordx4 v[216:219], v232, s[62:63] nt
	v_add_u32_e32 v233, 0x200000, v232
	global_load_dwordx4 v[220:223], v233, s[62:63] nt
	v_add_u32_e32 v233, 0x400000, v232
	global_load_dwordx4 v[224:227], v233, s[62:63] nt
	v_add_u32_e32 v233, 0x600000, v232
	global_load_dwordx4 v[228:231], v233, s[62:63] nt
	v_lshl_add_u32 v42, v46, 1, 0
	s_movk_i32 s3, 0x110
	v_mad_u32_u24 v43, v44, s3, v42
	s_waitcnt vmcnt(13)
	ds_write_b128 v43, v[6:9]
	v_mad_u32_u24 v6, v45, s3, v42
	s_waitcnt vmcnt(12)
	ds_write_b128 v6, v[2:5]
	v_mad_u32_u24 v2, v47, s3, v42
	s_waitcnt vmcnt(11)
	ds_write_b128 v2, v[14:17]
	v_mad_u32_u24 v2, v48, s3, v42
	s_waitcnt vmcnt(10)
	ds_write_b128 v2, v[10:13]
	v_mad_u32_u24 v2, v49, s3, v42
	s_waitcnt vmcnt(9)
	ds_write_b128 v2, v[22:25]
	v_lshrrev_b32_e32 v2, 4, v120
	s_movk_i32 s0, 0xe10
	s_lshl_b64 s[4:5], s[86:87], 19
	v_mad_u32_u24 v2, v2, s3, v42
	v_cmp_gt_u32_e32 vcc, s0, v1
	s_waitcnt vmcnt(8)
	ds_write_b128 v2, v[18:21]
	s_and_saveexec_b64 s[0:1], vcc
	s_cbranch_execz .LBB2_104
	v_lshrrev_b32_e32 v1, 4, v1
	v_mad_u32_u24 v1, v1, s3, v42
	s_waitcnt vmcnt(7)
	ds_write_b128 v1, v[30:33]
.LBB2_104:
	s_or_b64 exec, exec, s[0:1]
	v_cmp_gt_u32_e32 vcc, 16, v0
	s_and_saveexec_b64 s[0:1], vcc
	s_cbranch_execz .LBB2_106
	s_waitcnt vmcnt(6)
	ds_write_b128 v42, v[26:29] offset:60928
.LBB2_106:
	s_or_b64 exec, exec, s[0:1]
	s_movk_i32 s0, 0x3c0
	v_cmp_gt_u32_e32 vcc, s0, v0
	s_and_saveexec_b64 s[0:1], vcc
	s_cbranch_execz .LBB2_108
	v_mul_u32_u24_e32 v1, 0x110, v44
	v_add_u32_e32 v1, v42, v1
	s_waitcnt vmcnt(5)
	ds_write_b128 v1, v[38:41] offset:61200
.LBB2_108:
	s_or_b64 exec, exec, s[0:1]
	s_movk_i32 s0, 0x1c0
	v_cmp_gt_u32_e32 vcc, s0, v0
	s_and_saveexec_b64 s[0:1], vcc
	s_cbranch_execz .LBB2_110
	v_mul_u32_u24_e32 v1, 0x110, v45
	v_add_u32_e32 v1, v42, v1
	s_waitcnt vmcnt(4)
	ds_write_b128 v1, v[34:37] offset:61200
.LBB2_110:
	s_or_b64 exec, exec, s[0:1]
	v_bfe_u32 v65, v0, 6, 1
	v_bfe_u32 v1, v0, 3, 1
	v_lshl_or_b32 v46, v65, 1, v1
	v_lshrrev_b32_e32 v1, 3, v0
	v_and_b32_e32 v97, 15, v0
	v_and_b32_e32 v1, 48, v1
	v_or_b32_e32 v63, v1, v97
	v_mul_lo_u16_e32 v2, 20, v63
	v_lshrrev_b16_e32 v2, 7, v2
	v_and_b32_e32 v2, 14, v2
	v_or_b32_e32 v110, 64, v63
	v_add_u32_sdwa v6, v63, v2 dst_sel:DWORD dst_unused:UNUSED_PAD src0_sel:DWORD src1_sel:WORD_0
	v_mul_lo_u16_e32 v2, 0x4f, v110
	v_lshrrev_b16_e32 v2, 9, v2
	v_and_b32_e32 v2, 62, v2
	v_bfe_u32 v62, v0, 4, 2
	v_and_b32_e32 v47, 7, v0
	v_add_u32_e32 v10, v110, v2
	v_lshl_add_u32 v84, v62, 4, 0
	v_mad_u32_u24 v2, v46, 10, v47
	s_movk_i32 s0, 0x110
	s_waitcnt vmcnt(0)
	v_mad_u32_u24 v34, v2, s0, v84
	s_waitcnt lgkmcnt(0)
	s_barrier
	ds_read_b128 v[2:5], v34 offset:61200
	v_or_b32_e32 v64, 0x80, v63
	v_min_u32_e32 v22, 0xa8, v64
	v_mul_lo_u16_e32 v7, 0x4f, v22
	v_lshrrev_b32_e32 v180, 4, v1
	v_lshrrev_b32_e32 v181, 1, v180
	v_and_b32_e32 v182, 1, v180
	v_lshl_or_b32 v181, v181, 5, v182
	v_add_u32_e32 v183, 4, v97
	v_add_u32_e32 v184, -8, v97
	v_cmp_gt_u32_e64 s[90:91], 4, v97
	v_cmp_lt_u32_e64 s[92:93], 11, v97
	v_mov_b32_e32 v188, 0xc0
	s_nop 0
	v_cndmask_b32_e64 v183, v183, v97, s[90:91]
	v_cndmask_b32_e64 v183, v183, v184, s[92:93]
	v_lshl_add_u32 v185, v183, 1, v181
	v_add_u32_e32 v186, 64, v185
	v_add_u32_e32 v187, 0x80, v185
	v_cmp_eq_u32_e32 vcc, 0xa4, v187
	s_nop 1
	v_cndmask_b32_e32 v187, v187, v188, vcc
	v_mul_u32_u24_e32 v189, 0x89, v185
	v_lshrrev_b32_e32 v189, 11, v189
	v_mad_i32_i24 v190, v189, -15, v185
	v_cmp_gt_u32_e32 vcc, 13, v190
	v_lshlrev_b32_e32 v191, 1, v189
	v_sub_u32_e32 v193, v185, v191
	v_mad_u32_u24 v98, v185, s0, v84
	v_cndmask_b32_e64 v196, 0, 1, vcc
	v_mul_u32_u24_e32 v189, 0x89, v186
	v_lshrrev_b32_e32 v189, 11, v189
	v_mad_i32_i24 v190, v189, -15, v186
	v_cmp_gt_u32_e32 vcc, 13, v190
	v_lshlrev_b32_e32 v191, 1, v189
	v_sub_u32_e32 v194, v186, v191
	v_mad_u32_u24 v111, v186, s0, v84
	v_cndmask_b32_e64 v197, 0, 1, vcc
	v_mul_u32_u24_e32 v189, 0x89, v187
	v_lshrrev_b32_e32 v189, 11, v189
	v_mad_i32_i24 v190, v189, -15, v187
	v_cmp_gt_u32_e32 vcc, 13, v190
	v_lshlrev_b32_e32 v191, 1, v189
	v_sub_u32_e32 v195, v187, v191
	v_mad_u32_u24 v117, v187, s0, v84
	v_cndmask_b32_e64 v198, 0, 1, vcc
	v_lshrrev_b16_e32 v23, 9, v7
	ds_read_b128 v[6:9], v98
	ds_read_b128 v[10:13], v111
	ds_read_b128 v[14:17], v34 offset:61264
	ds_read_b128 v[18:21], v98 offset:64
	v_and_b32_e32 v23, 30, v23
	s_waitcnt lgkmcnt(3)
	v_mfma_f32_16x16x32_f16 v[6:9], v[2:5], v[6:9], 0
	v_add_u32_e32 v26, v22, v23
	ds_read_b128 v[22:25], v111 offset:64
	ds_read_b128 v[26:29], v117
	ds_read_b128 v[30:33], v117 offset:64
	s_waitcnt lgkmcnt(3)
	v_mfma_f32_16x16x32_f16 v[6:9], v[14:17], v[18:21], v[6:9]
	ds_read_b128 v[18:21], v34 offset:61328
	v_add_u32_e32 v58, 1, v47
	v_add_u32_e32 v85, 2, v47
	v_mfma_f32_16x16x32_f16 v[10:13], v[2:5], v[10:13], 0
	v_lshl_or_b32 v86, s2, 9, v0
	v_ashrrev_i32_e32 v87, 31, v86
	v_lshlrev_b64 v[74:75], 4, v[86:87]
	s_waitcnt lgkmcnt(2)
	v_mfma_f32_16x16x32_f16 v[2:5], v[2:5], v[26:29], 0
	v_mad_u32_u24 v90, v46, 10, 20
	v_lshl_add_u64 v[70:71], s[60:61], 0, v[74:75]
	v_add_co_u32_e32 v42, vcc, 0x200000, v70
	v_mfma_f32_16x16x32_f16 v[10:13], v[14:17], v[22:25], v[10:13]
	s_nop 0
	v_addc_co_u32_e32 v43, vcc, 0, v71, vcc
	v_add_co_u32_e32 v50, vcc, 0x400000, v70
	s_waitcnt lgkmcnt(1)
	v_mfma_f32_16x16x32_f16 v[2:5], v[14:17], v[30:33], v[2:5]
	ds_read_b128 v[14:17], v98 offset:128
	ds_read_b128 v[22:25], v34 offset:61392
	ds_read_b128 v[26:29], v98 offset:192
	v_addc_co_u32_e32 v51, vcc, 0, v71, vcc
	s_waitcnt lgkmcnt(2)
	v_mfma_f32_16x16x32_f16 v[6:9], v[18:21], v[14:17], v[6:9]
	ds_read_b128 v[14:17], v111 offset:128
	ds_read_b128 v[30:33], v111 offset:192
	v_add_co_u32_e32 v52, vcc, 0x600000, v70
	s_waitcnt lgkmcnt(1)
	v_mfma_f32_16x16x32_f16 v[10:13], v[18:21], v[14:17], v[10:13]
	ds_read_b128 v[14:17], v117 offset:128
	ds_read_b128 v[34:37], v117 offset:192
	v_addc_co_u32_e32 v53, vcc, 0, v71, vcc
	s_waitcnt lgkmcnt(1)
	v_mfma_f32_16x16x32_f16 v[2:5], v[18:21], v[14:17], v[2:5]
	v_mad_u32_u24 v14, v46, 10, v58
	v_mad_u32_u24 v38, v14, s0, v84
	ds_read_b128 v[14:17], v38 offset:61200
	v_mfma_f32_16x16x32_f16 v[6:9], v[22:25], v[26:29], v[6:9]
	v_add_co_u32_e32 v54, vcc, 0x800000, v70
	s_mov_b32 s1, 0x200000
	v_mfma_f32_16x16x32_f16 v[10:13], v[22:25], v[30:33], v[10:13]
	v_addc_co_u32_e32 v55, vcc, 0, v71, vcc
	v_lshl_add_u64 v[82:83], s[62:63], 0, v[74:75]
	s_waitcnt lgkmcnt(1)
	v_mfma_f32_16x16x32_f16 v[2:5], v[22:25], v[34:37], v[2:5]
	ds_read_b128 v[18:21], v98 offset:272
	ds_read_b128 v[22:25], v38 offset:61264
	ds_read_b128 v[26:29], v98 offset:336
	s_mov_b32 s2, 0x400000
	s_mov_b32 s3, 0x600000
	s_waitcnt lgkmcnt(2)
	v_mfma_f32_16x16x32_f16 v[6:9], v[14:17], v[18:21], v[6:9]
	ds_read_b128 v[18:21], v111 offset:272
	ds_read_b128 v[30:33], v111 offset:336
	s_add_i32 s6, 0, 0x13890
	s_waitcnt lgkmcnt(1)
	v_mfma_f32_16x16x32_f16 v[10:13], v[14:17], v[18:21], v[10:13]
	ds_read_b128 v[18:21], v117 offset:272
	ds_read_b128 v[34:37], v117 offset:336
	s_waitcnt lgkmcnt(1)
	v_mfma_f32_16x16x32_f16 v[2:5], v[14:17], v[18:21], v[2:5]
	ds_read_b128 v[14:17], v38 offset:61328
	v_mfma_f32_16x16x32_f16 v[6:9], v[22:25], v[26:29], v[6:9]
	v_mfma_f32_16x16x32_f16 v[10:13], v[22:25], v[30:33], v[10:13]
	s_waitcnt lgkmcnt(1)
	v_mfma_f32_16x16x32_f16 v[2:5], v[22:25], v[34:37], v[2:5]
	ds_read_b128 v[18:21], v98 offset:400
	ds_read_b128 v[22:25], v38 offset:61392
	ds_read_b128 v[26:29], v98 offset:464
	s_waitcnt lgkmcnt(2)
	v_mfma_f32_16x16x32_f16 v[6:9], v[14:17], v[18:21], v[6:9]
	ds_read_b128 v[18:21], v111 offset:400
	ds_read_b128 v[30:33], v111 offset:464
	s_waitcnt lgkmcnt(1)
	v_mfma_f32_16x16x32_f16 v[10:13], v[14:17], v[18:21], v[10:13]
	ds_read_b128 v[18:21], v117 offset:400
	ds_read_b128 v[34:37], v117 offset:464
	s_waitcnt lgkmcnt(1)
	v_mfma_f32_16x16x32_f16 v[2:5], v[14:17], v[18:21], v[2:5]
	v_mad_u32_u24 v14, v46, 10, v85
	v_mad_u32_u24 v38, v14, s0, v84
	ds_read_b128 v[14:17], v38 offset:61200
	v_mfma_f32_16x16x32_f16 v[6:9], v[22:25], v[26:29], v[6:9]
	v_mfma_f32_16x16x32_f16 v[10:13], v[22:25], v[30:33], v[10:13]
	s_waitcnt lgkmcnt(1)
	v_mfma_f32_16x16x32_f16 v[2:5], v[22:25], v[34:37], v[2:5]
	ds_read_b128 v[18:21], v98 offset:544
	ds_read_b128 v[22:25], v38 offset:61264
	ds_read_b128 v[26:29], v98 offset:608
	s_waitcnt lgkmcnt(2)
	v_mfma_f32_16x16x32_f16 v[6:9], v[14:17], v[18:21], v[6:9]
	ds_read_b128 v[18:21], v111 offset:544
	ds_read_b128 v[30:33], v111 offset:608
	s_waitcnt lgkmcnt(1)
	v_mfma_f32_16x16x32_f16 v[10:13], v[14:17], v[18:21], v[10:13]
	ds_read_b128 v[18:21], v117 offset:544
	ds_read_b128 v[34:37], v117 offset:608
	s_waitcnt lgkmcnt(1)
	v_mfma_f32_16x16x32_f16 v[2:5], v[14:17], v[18:21], v[2:5]
	ds_read_b128 v[14:17], v38 offset:61328
	v_mfma_f32_16x16x32_f16 v[6:9], v[22:25], v[26:29], v[6:9]
	v_mfma_f32_16x16x32_f16 v[10:13], v[22:25], v[30:33], v[10:13]
	s_waitcnt lgkmcnt(1)
	v_mfma_f32_16x16x32_f16 v[2:5], v[22:25], v[34:37], v[2:5]
	ds_read_b128 v[18:21], v98 offset:672
	ds_read_b128 v[22:25], v38 offset:61392
	ds_read_b128 v[26:29], v98 offset:736
	v_mad_u32_u24 v38, v46, 10, 10
	s_waitcnt lgkmcnt(2)
	v_mfma_f32_16x16x32_f16 v[6:9], v[14:17], v[18:21], v[6:9]
	ds_read_b128 v[18:21], v111 offset:672
	ds_read_b128 v[30:33], v111 offset:736
	s_waitcnt lgkmcnt(1)
	v_mfma_f32_16x16x32_f16 v[10:13], v[14:17], v[18:21], v[10:13]
	ds_read_b128 v[18:21], v117 offset:672
	ds_read_b128 v[34:37], v117 offset:736
	s_waitcnt lgkmcnt(1)
	v_mfma_f32_16x16x32_f16 v[2:5], v[14:17], v[18:21], v[2:5]
	v_add_u32_e32 v14, v47, v38
	v_mad_u32_u24 v39, v14, s0, v84
	ds_read_b128 v[14:17], v39 offset:61200
	v_mfma_f32_16x16x32_f16 v[6:9], v[22:25], v[26:29], v[6:9]
	v_mfma_f32_16x16x32_f16 v[10:13], v[22:25], v[30:33], v[10:13]
	s_waitcnt lgkmcnt(1)
	v_mfma_f32_16x16x32_f16 v[2:5], v[22:25], v[34:37], v[2:5]
	ds_read_b128 v[18:21], v98 offset:4080
	ds_read_b128 v[22:25], v39 offset:61264
	ds_read_b128 v[26:29], v98 offset:4144
	s_waitcnt lgkmcnt(2)
	v_mfma_f32_16x16x32_f16 v[6:9], v[14:17], v[18:21], v[6:9]
	ds_read_b128 v[18:21], v111 offset:4080
	ds_read_b128 v[30:33], v111 offset:4144
	s_waitcnt lgkmcnt(1)
	v_mfma_f32_16x16x32_f16 v[10:13], v[14:17], v[18:21], v[10:13]
	ds_read_b128 v[18:21], v117 offset:4080
	ds_read_b128 v[34:37], v117 offset:4144
	s_waitcnt lgkmcnt(1)
	v_mfma_f32_16x16x32_f16 v[2:5], v[14:17], v[18:21], v[2:5]
	ds_read_b128 v[14:17], v39 offset:61328
	v_mfma_f32_16x16x32_f16 v[6:9], v[22:25], v[26:29], v[6:9]
	v_mfma_f32_16x16x32_f16 v[10:13], v[22:25], v[30:33], v[10:13]
	s_waitcnt lgkmcnt(1)
	v_mfma_f32_16x16x32_f16 v[2:5], v[22:25], v[34:37], v[2:5]
	ds_read_b128 v[18:21], v98 offset:4208
	ds_read_b128 v[22:25], v39 offset:61392
	ds_read_b128 v[26:29], v98 offset:4272
	s_waitcnt lgkmcnt(2)
	v_mfma_f32_16x16x32_f16 v[6:9], v[14:17], v[18:21], v[6:9]
	ds_read_b128 v[18:21], v111 offset:4208
	ds_read_b128 v[30:33], v111 offset:4272
	s_waitcnt lgkmcnt(1)
	v_mfma_f32_16x16x32_f16 v[10:13], v[14:17], v[18:21], v[10:13]
	ds_read_b128 v[18:21], v117 offset:4208
	ds_read_b128 v[34:37], v117 offset:4272
	s_waitcnt lgkmcnt(1)
	v_mfma_f32_16x16x32_f16 v[2:5], v[14:17], v[18:21], v[2:5]
	v_add_u32_e32 v14, v58, v38
	v_mad_u32_u24 v39, v14, s0, v84
	ds_read_b128 v[14:17], v39 offset:61200
	v_mfma_f32_16x16x32_f16 v[6:9], v[22:25], v[26:29], v[6:9]
	v_mfma_f32_16x16x32_f16 v[10:13], v[22:25], v[30:33], v[10:13]
	s_waitcnt lgkmcnt(1)
	v_mfma_f32_16x16x32_f16 v[2:5], v[22:25], v[34:37], v[2:5]
	ds_read_b128 v[18:21], v98 offset:4352
	ds_read_b128 v[22:25], v39 offset:61264
	ds_read_b128 v[26:29], v98 offset:4416
	s_waitcnt lgkmcnt(2)
	v_mfma_f32_16x16x32_f16 v[6:9], v[14:17], v[18:21], v[6:9]
	ds_read_b128 v[18:21], v111 offset:4352
	ds_read_b128 v[30:33], v111 offset:4416
	s_waitcnt lgkmcnt(1)
	v_mfma_f32_16x16x32_f16 v[10:13], v[14:17], v[18:21], v[10:13]
	ds_read_b128 v[18:21], v117 offset:4352
	ds_read_b128 v[34:37], v117 offset:4416
	s_waitcnt lgkmcnt(1)
	v_mfma_f32_16x16x32_f16 v[2:5], v[14:17], v[18:21], v[2:5]
	ds_read_b128 v[14:17], v39 offset:61328
	v_mfma_f32_16x16x32_f16 v[6:9], v[22:25], v[26:29], v[6:9]
	v_mfma_f32_16x16x32_f16 v[10:13], v[22:25], v[30:33], v[10:13]
	s_waitcnt lgkmcnt(1)
	v_mfma_f32_16x16x32_f16 v[2:5], v[22:25], v[34:37], v[2:5]
	ds_read_b128 v[18:21], v98 offset:4480
	ds_read_b128 v[22:25], v39 offset:61392
	ds_read_b128 v[26:29], v98 offset:4544
	s_waitcnt lgkmcnt(2)
	v_mfma_f32_16x16x32_f16 v[6:9], v[14:17], v[18:21], v[6:9]
	ds_read_b128 v[18:21], v111 offset:4480
	ds_read_b128 v[30:33], v111 offset:4544
	s_waitcnt lgkmcnt(1)
	v_mfma_f32_16x16x32_f16 v[10:13], v[14:17], v[18:21], v[10:13]
	ds_read_b128 v[18:21], v117 offset:4480
	ds_read_b128 v[34:37], v117 offset:4544
	s_waitcnt lgkmcnt(1)
	v_mfma_f32_16x16x32_f16 v[2:5], v[14:17], v[18:21], v[2:5]
	v_add_u32_e32 v14, v85, v38
	v_mad_u32_u24 v38, v14, s0, v84
	ds_read_b128 v[14:17], v38 offset:61200
	v_mfma_f32_16x16x32_f16 v[6:9], v[22:25], v[26:29], v[6:9]
	v_mfma_f32_16x16x32_f16 v[10:13], v[22:25], v[30:33], v[10:13]
	s_waitcnt lgkmcnt(1)
	v_mfma_f32_16x16x32_f16 v[2:5], v[22:25], v[34:37], v[2:5]
	ds_read_b128 v[18:21], v98 offset:4624
	ds_read_b128 v[22:25], v38 offset:61264
	ds_read_b128 v[26:29], v98 offset:4688
	s_waitcnt lgkmcnt(2)
	v_mfma_f32_16x16x32_f16 v[6:9], v[14:17], v[18:21], v[6:9]
	ds_read_b128 v[18:21], v111 offset:4624
	ds_read_b128 v[30:33], v111 offset:4688
	s_waitcnt lgkmcnt(1)
	v_mfma_f32_16x16x32_f16 v[10:13], v[14:17], v[18:21], v[10:13]
	ds_read_b128 v[18:21], v117 offset:4624
	ds_read_b128 v[34:37], v117 offset:4688
	s_waitcnt lgkmcnt(1)
	v_mfma_f32_16x16x32_f16 v[2:5], v[14:17], v[18:21], v[2:5]
	ds_read_b128 v[14:17], v38 offset:61328
	ds_read_b128 v[18:21], v98 offset:4752
	v_mfma_f32_16x16x32_f16 v[6:9], v[22:25], v[26:29], v[6:9]
	v_mfma_f32_16x16x32_f16 v[10:13], v[22:25], v[30:33], v[10:13]
	s_waitcnt lgkmcnt(2)
	v_mfma_f32_16x16x32_f16 v[22:25], v[22:25], v[34:37], v[2:5]
	s_nop 2
	ds_read_b128 v[2:5], v111 offset:4752
	ds_read_b128 v[26:29], v38 offset:61392
	ds_read_b128 v[30:33], v98 offset:4816
	ds_read_b128 v[34:37], v117 offset:4752
	ds_read_b128 v[38:41], v111 offset:4816
	s_waitcnt lgkmcnt(5)
	v_mfma_f32_16x16x32_f16 v[18:21], v[14:17], v[18:21], v[6:9]
	s_waitcnt lgkmcnt(4)
	v_mfma_f32_16x16x32_f16 v[10:13], v[14:17], v[2:5], v[10:13]
	s_nop 0
	global_load_dwordx4 v[6:9], v[70:71], off nt
	global_load_dwordx4 v[2:5], v[42:43], off nt
	ds_read_b128 v[42:45], v117 offset:4816
	s_waitcnt lgkmcnt(2)
	v_mfma_f32_16x16x32_f16 v[14:17], v[14:17], v[34:37], v[22:25]
	s_nop 2
	v_add_u32_e32 v22, v47, v90
	v_mad_u32_u24 v56, v22, s0, v84
	ds_read_b128 v[22:25], v56 offset:61200
	v_mfma_f32_16x16x32_f16 v[18:21], v[26:29], v[30:33], v[18:21]
	ds_read_b128 v[30:33], v98 offset:8160
	s_waitcnt lgkmcnt(3)
	v_mfma_f32_16x16x32_f16 v[10:13], v[26:29], v[38:41], v[10:13]
	s_waitcnt lgkmcnt(2)
	v_mfma_f32_16x16x32_f16 v[14:17], v[26:29], v[42:45], v[14:17]
	ds_read_b128 v[26:29], v111 offset:8160
	ds_read_b128 v[34:37], v56 offset:61264
	ds_read_b128 v[38:41], v98 offset:8224
	s_waitcnt lgkmcnt(3)
	v_mfma_f32_16x16x32_f16 v[18:21], v[22:25], v[30:33], v[18:21]
	ds_read_b128 v[30:33], v117 offset:8160
	ds_read_b128 v[42:45], v111 offset:8224
	ds_read_b128 v[46:49], v117 offset:8224
	s_waitcnt lgkmcnt(5)
	v_mfma_f32_16x16x32_f16 v[26:29], v[22:25], v[26:29], v[10:13]
	s_waitcnt lgkmcnt(2)
	v_mfma_f32_16x16x32_f16 v[22:25], v[22:25], v[30:33], v[14:17]
	s_nop 2
	global_load_dwordx4 v[14:17], v[50:51], off nt
	global_load_dwordx4 v[10:13], v[52:53], off nt
	ds_read_b128 v[30:33], v56 offset:61328
	v_mfma_f32_16x16x32_f16 v[18:21], v[34:37], v[38:41], v[18:21]
	ds_read_b128 v[38:41], v98 offset:8288
	s_waitcnt lgkmcnt(3)
	v_mfma_f32_16x16x32_f16 v[26:29], v[34:37], v[42:45], v[26:29]
	s_waitcnt lgkmcnt(2)
	v_mfma_f32_16x16x32_f16 v[22:25], v[34:37], v[46:49], v[22:25]
	ds_read_b128 v[34:37], v111 offset:8288
	ds_read_b128 v[42:45], v56 offset:61392
	ds_read_b128 v[46:49], v98 offset:8352
	v_add_co_u32_e32 v56, vcc, 0xa00000, v70
	s_waitcnt lgkmcnt(3)
	v_mfma_f32_16x16x32_f16 v[38:41], v[30:33], v[38:41], v[18:21]
	s_nop 2
	ds_read_b128 v[18:21], v117 offset:8288
	ds_read_b128 v[50:53], v111 offset:8352
	v_addc_co_u32_e32 v57, vcc, 0, v71, vcc
	s_waitcnt lgkmcnt(2)
	v_mfma_f32_16x16x32_f16 v[38:41], v[42:45], v[46:49], v[38:41]
	v_add_u32_e32 v46, v58, v90
	v_mad_u32_u24 v80, v46, s0, v84
	v_add_co_u32_e32 v76, vcc, 0xc00000, v70
	v_mfma_f32_16x16x32_f16 v[26:29], v[30:33], v[34:37], v[26:29]
	ds_read_b128 v[34:37], v117 offset:8352
	v_addc_co_u32_e32 v77, vcc, 0, v71, vcc
	s_waitcnt lgkmcnt(2)
	v_mfma_f32_16x16x32_f16 v[30:33], v[30:33], v[18:21], v[22:25]
	s_nop 2
	global_load_dwordx4 v[22:25], v[54:55], off nt
	global_load_dwordx4 v[18:21], v[56:57], off nt
	ds_read_b128 v[46:49], v80 offset:61200
	v_add_co_u32_e32 v78, vcc, 0xe00000, v70
	s_waitcnt lgkmcnt(2)
	v_mfma_f32_16x16x32_f16 v[26:29], v[42:45], v[50:53], v[26:29]
	ds_read_b128 v[50:53], v98 offset:8432
	v_addc_co_u32_e32 v79, vcc, 0, v71, vcc
	s_waitcnt lgkmcnt(2)
	v_mfma_f32_16x16x32_f16 v[30:33], v[42:45], v[34:37], v[30:33]
	ds_read_b128 v[34:37], v111 offset:8432
	ds_read_b128 v[42:45], v80 offset:61264
	ds_read_b128 v[54:57], v98 offset:8496
	v_add_co_u32_e32 v74, vcc, s1, v82
	s_waitcnt lgkmcnt(3)
	v_mfma_f32_16x16x32_f16 v[38:41], v[46:49], v[50:53], v[38:41]
	ds_read_b128 v[50:53], v117 offset:8432
	ds_read_b128 v[58:61], v111 offset:8496
	ds_read_b128 v[70:73], v117 offset:8496
	v_addc_co_u32_e32 v75, vcc, 0, v83, vcc
	s_waitcnt lgkmcnt(5)
	v_mfma_f32_16x16x32_f16 v[66:69], v[46:49], v[34:37], v[26:29]
	global_load_dwordx4 v[34:37], v[76:77], off nt
	s_nop 1
	global_load_dwordx4 v[26:29], v[78:79], off nt
	v_add_co_u32_e32 v88, vcc, s2, v82
	s_waitcnt lgkmcnt(2)
	v_mfma_f32_16x16x32_f16 v[30:33], v[46:49], v[50:53], v[30:33]
	ds_read_b128 v[46:49], v80 offset:61328
	v_addc_co_u32_e32 v89, vcc, 0, v83, vcc
	v_mfma_f32_16x16x32_f16 v[38:41], v[42:45], v[54:57], v[38:41]
	ds_read_b128 v[54:57], v98 offset:8560
	s_movk_i32 s2, 0xa9
	s_waitcnt lgkmcnt(3)
	v_mfma_f32_16x16x32_f16 v[50:53], v[42:45], v[58:61], v[66:69]
	s_waitcnt lgkmcnt(2)
	v_mfma_f32_16x16x32_f16 v[42:45], v[42:45], v[70:73], v[30:33]
	ds_read_b128 v[58:61], v111 offset:8560
	ds_read_b128 v[66:69], v80 offset:61392
	ds_read_b128 v[70:73], v98 offset:8624
	s_waitcnt lgkmcnt(3)
	v_mfma_f32_16x16x32_f16 v[54:57], v[46:49], v[54:57], v[38:41]
	s_nop 2
	ds_read_b128 v[74:77], v117 offset:8560
	ds_read_b128 v[78:81], v111 offset:8624
	s_waitcnt lgkmcnt(4)
	v_mfma_f32_16x16x32_f16 v[50:53], v[46:49], v[58:61], v[50:53]
	ds_read_b128 v[58:61], v117 offset:8624
	s_waitcnt lgkmcnt(2)
	v_mfma_f32_16x16x32_f16 v[42:45], v[46:49], v[74:77], v[42:45]
	v_mfma_f32_16x16x32_f16 v[46:49], v[66:69], v[70:73], v[54:57]
	ds_read_b128 v[70:73], v98 offset:8704
	s_nop 1
	v_add_u32_e32 v54, v85, v90
	v_mad_u32_u24 v92, v54, s0, v84
	ds_read_b128 v[54:57], v92 offset:61200
	s_waitcnt lgkmcnt(3)
	v_mfma_f32_16x16x32_f16 v[50:53], v[66:69], v[78:81], v[50:53]
	v_add_co_u32_e32 v90, vcc, s3, v82
	s_add_i32 s0, 0, 0x13550
	s_waitcnt lgkmcnt(2)
	v_mfma_f32_16x16x32_f16 v[58:61], v[66:69], v[58:61], v[42:45]
	s_nop 2
	ds_read_b128 v[42:45], v111 offset:8704
	ds_read_b128 v[66:69], v92 offset:61264
	ds_read_b128 v[74:77], v98 offset:8768
	v_addc_co_u32_e32 v91, vcc, 0, v83, vcc
	s_waitcnt lgkmcnt(3)
	v_mfma_f32_16x16x32_f16 v[70:73], v[54:57], v[70:73], v[46:49]
	ds_read_b128 v[78:81], v117 offset:8704
	ds_read_b128 v[82:85], v111 offset:8768
	v_cmp_gt_u32_e64 s[2:3], s2, v64
	v_cmp_eq_u32_e32 vcc, 0, v97
	s_waitcnt lgkmcnt(4)
	v_mfma_f32_16x16x32_f16 v[50:53], v[54:57], v[42:45], v[50:53]
	ds_read_b128 v[88:91], v117 offset:8768
	s_waitcnt lgkmcnt(2)
	v_mfma_f32_16x16x32_f16 v[54:57], v[54:57], v[78:81], v[58:61]
	s_nop 2
	ds_read_b128 v[58:61], v92 offset:61328
	ds_read_b128 v[92:95], v92 offset:61392
	ds_read_b128 v[78:81], v98 offset:8832
	ds_read_b128 v[98:101], v98 offset:8896
	ds_read_b128 v[106:109], v111 offset:8832
	ds_read_b128 v[118:121], v111 offset:8896
	ds_read_b128 v[122:125], v117 offset:8832
	ds_read_b128 v[126:129], v117 offset:8896
	v_mfma_f32_16x16x32_f16 v[102:105], v[66:69], v[74:77], v[70:73]
	s_waitcnt lgkmcnt(9)
	v_mfma_f32_16x16x32_f16 v[50:53], v[66:69], v[82:85], v[50:53]
	s_nop 0
	v_lshlrev_b32_e32 v70, 2, v62
	v_lshl_or_b32 v73, v65, 4, v70
	v_lshl_add_u32 v75, v73, 2, 0
	s_waitcnt lgkmcnt(8)
	v_mfma_f32_16x16x32_f16 v[66:69], v[66:69], v[88:91], v[54:57]
	v_add_u32_e32 v65, 0x13810, v75
	v_min_u32_e32 v72, 0xaf, v64
	v_lshl_add_u32 v70, v63, 2, s0
	s_waitcnt lgkmcnt(5)
	v_mfma_f32_16x16x32_f16 v[54:57], v[58:61], v[78:81], v[102:105]
	v_lshl_add_u32 v71, v110, 2, s0
	v_lshl_add_u32 v72, v72, 2, s0
	ds_read_b32 v65, v65
	ds_read_b32 v79, v70
	ds_read_b32 v78, v71
	ds_read_b32 v77, v72
	s_waitcnt lgkmcnt(7)
	v_mfma_f32_16x16x32_f16 v[80:83], v[58:61], v[106:109], v[50:53]
	s_movk_i32 s0, 0x69
	v_cmp_gt_u32_e64 s[0:1], s0, v63
	s_waitcnt lgkmcnt(5)
	v_mfma_f32_16x16x32_f16 v[58:61], v[58:61], v[122:125], v[66:69]
	v_mfma_f32_16x16x32_f16 v[50:53], v[92:95], v[98:101], v[54:57]
	v_mfma_f32_16x16x32_f16 v[54:57], v[92:95], v[118:121], v[80:83]
	s_waitcnt lgkmcnt(4)
	v_mfma_f32_16x16x32_f16 v[58:61], v[92:95], v[126:129], v[58:61]
	s_waitcnt lgkmcnt(2)
	s_nop 3
	v_or_b32_e32 v69, 1, v73
	v_or_b32_e32 v64, 2, v73
	v_or_b32_e32 v152, 3, v73
	v_lshl_add_u32 v71, v69, 2, 0
	v_lshl_add_u32 v66, v64, 2, 0
	v_lshl_add_u32 v153, v152, 2, 0
	v_add_u32_e32 v160, 0x13810, v71
	v_add_u32_e32 v161, 0x13810, v66
	v_add_u32_e32 v162, 0x13810, v153
	v_mov_b32_e32 v156, 0x13550
	v_lshl_add_u32 v157, v193, 2, v156
	v_lshl_add_u32 v158, v194, 2, v156
	v_lshl_add_u32 v159, v195, 2, v156
	ds_read_b32 v79, v157
	ds_read_b32 v78, v158
	ds_read_b32 v77, v159
	ds_read_b32 v160, v160
	ds_read_b32 v161, v161
	ds_read_b32 v162, v162
	v_mov_b32_e32 v155, 0xff800000
	s_waitcnt lgkmcnt(3)
	v_mul_f32_e32 v164, v50, v79
	v_mul_f32_e32 v165, v54, v78
	v_mul_f32_e32 v166, v58, v77
	v_mul_f32_e32 v164, v65, v164
	v_mul_f32_e32 v165, v65, v165
	v_mul_f32_e32 v166, v65, v166
	v_mul_f32_e32 v167, v51, v79
	v_mul_f32_e32 v168, v55, v78
	v_mul_f32_e32 v169, v59, v77
	v_mul_f32_e32 v170, v52, v79
	v_mul_f32_e32 v171, v56, v78
	v_mul_f32_e32 v172, v60, v77
	v_mul_f32_e32 v173, v53, v79
	v_mul_f32_e32 v174, v57, v78
	v_mul_f32_e32 v175, v61, v77
	s_waitcnt lgkmcnt(0)
	v_mul_f32_e32 v167, v160, v167
	v_mul_f32_e32 v168, v160, v168
	v_mul_f32_e32 v169, v160, v169
	v_mul_f32_e32 v170, v161, v170
	v_mul_f32_e32 v171, v161, v171
	v_mul_f32_e32 v172, v161, v172
	v_mul_f32_e32 v173, v162, v173
	v_mul_f32_e32 v174, v162, v174
	v_mul_f32_e32 v175, v162, v175
	v_cmp_ne_u32_e64 s[8:9], 0, v196
	v_cmp_ne_u32_e64 s[0:1], 0, v197
	v_cmp_ne_u32_e64 s[2:3], 0, v198
	v_cndmask_b32_e64 v164, v155, v164, s[8:9]
	v_cndmask_b32_e64 v167, v155, v167, s[8:9]
	v_cndmask_b32_e64 v170, v155, v170, s[8:9]
	v_cndmask_b32_e64 v173, v155, v173, s[8:9]
	v_cndmask_b32_e64 v165, v155, v165, s[0:1]
	v_cndmask_b32_e64 v166, v155, v166, s[2:3]
	v_cndmask_b32_e64 v168, v155, v168, s[0:1]
	v_cndmask_b32_e64 v169, v155, v169, s[2:3]
	v_cndmask_b32_e64 v171, v155, v171, s[0:1]
	v_cndmask_b32_e64 v172, v155, v172, s[2:3]
	v_cndmask_b32_e64 v174, v155, v174, s[0:1]
	v_cndmask_b32_e64 v175, v155, v175, s[2:3]
	v_max_f32_e32 v176, 0xff800000, v164
	v_max_f32_e32 v177, 0xff800000, v167
	v_max_f32_e32 v178, 0xff800000, v170
	v_max_f32_e32 v179, 0xff800000, v173
	v_max3_f32 v176, v176, v165, v166
	v_max3_f32 v177, v177, v168, v169
	v_max3_f32 v178, v178, v171, v172
	v_max3_f32 v179, v179, v174, v175
	v_max_f32_dpp v176, v176, v176 quad_perm:[1,0,3,2] row_mask:0xf bank_mask:0xf
	v_max_f32_dpp v177, v177, v177 quad_perm:[1,0,3,2] row_mask:0xf bank_mask:0xf
	v_max_f32_dpp v178, v178, v178 quad_perm:[1,0,3,2] row_mask:0xf bank_mask:0xf
	v_max_f32_dpp v179, v179, v179 quad_perm:[1,0,3,2] row_mask:0xf bank_mask:0xf
	v_max_f32_dpp v176, v176, v176 quad_perm:[2,3,0,1] row_mask:0xf bank_mask:0xf
	v_max_f32_dpp v177, v177, v177 quad_perm:[2,3,0,1] row_mask:0xf bank_mask:0xf
	v_max_f32_dpp v178, v178, v178 quad_perm:[2,3,0,1] row_mask:0xf bank_mask:0xf
	v_max_f32_dpp v179, v179, v179 quad_perm:[2,3,0,1] row_mask:0xf bank_mask:0xf
	v_max_f32_dpp v176, v176, v176 row_half_mirror row_mask:0xf bank_mask:0xf
	v_max_f32_dpp v177, v177, v177 row_half_mirror row_mask:0xf bank_mask:0xf
	v_max_f32_dpp v178, v178, v178 row_half_mirror row_mask:0xf bank_mask:0xf
	v_max_f32_dpp v179, v179, v179 row_half_mirror row_mask:0xf bank_mask:0xf
	v_max_f32_dpp v176, v176, v176 row_mirror row_mask:0xf bank_mask:0xf
	v_max_f32_dpp v177, v177, v177 row_mirror row_mask:0xf bank_mask:0xf
	v_max_f32_dpp v178, v178, v178 row_mirror row_mask:0xf bank_mask:0xf
	v_max_f32_dpp v179, v179, v179 row_mirror row_mask:0xf bank_mask:0xf
	v_and_b32_e32 v58, 0x180, v0
	v_add_u32_e32 v58, s6, v58
	v_lshl_add_u32 v58, v73, 2, v58
	s_and_saveexec_b64 s[6:7], vcc
	ds_write_b128 v58, v[176:179]
	s_or_b64 exec, exec, s[6:7]
	v_mov_b32_e32 v76, v164
	v_mov_b32_e32 v74, v165
	v_mov_b32_e32 v72, v166
	v_mov_b32_e32 v70, v167
	v_mov_b32_e32 v68, v168
	v_mov_b32_e32 v67, v169
	v_mov_b32_e32 v65, v170
	v_mov_b32_e32 v59, v171
	v_mov_b32_e32 v56, v172
	v_mov_b32_e32 v53, v173
	v_mov_b32_e32 v52, v174
	v_mov_b32_e32 v50, v175
	v_mov_b32_e32 v54, v152
	v_mov_b32_e32 v55, v153
	v_add_u32_e32 v51, 0x13890, v75
	s_waitcnt lgkmcnt(0)
	s_barrier
	v_add_u32_e32 v152, 0x13890, v75
	ds_read_b128 v[156:159], v152
	ds_read_b128 v[160:163], v152 offset:128
	ds_read_b128 v[164:167], v152 offset:256
	ds_read_b128 v[168:171], v152 offset:384
	v_lshlrev_b32_e32 v51, 3, v62
	v_lshlrev_b32_e32 v60, 8, v73
	v_or_b32_e32 v172, v63, v60
	s_waitcnt lgkmcnt(0)
	v_max_f32_e32 v173, v156, v160
	v_max_f32_e32 v174, v157, v161
	v_max_f32_e32 v175, v158, v162
	v_max_f32_e32 v176, v159, v163
	v_max3_f32 v173, v173, v164, v168
	v_max3_f32 v174, v174, v165, v169
	v_max3_f32 v175, v175, v166, v170
	v_max3_f32 v176, v176, v167, v171
	v_add_f32_e32 v173, 0xbb102de0, v173
	v_add_f32_e32 v174, 0xbb102de0, v174
	v_add_f32_e32 v175, 0xbb102de0, v175
	v_add_f32_e32 v176, 0xbb102de0, v176
	v_cmp_ge_f32_e64 s[90:91], v76, v173
	v_cmp_ge_f32_e64 s[92:93], v74, v173
	v_cmp_ge_f32_e64 s[94:95], v72, v173
	v_cmp_ge_f32_e64 s[96:97], v70, v174
	v_cmp_ge_f32_e64 s[98:99], v68, v174
	v_cmp_ge_f32_e64 s[60:61], v67, v174
	v_cmp_ge_f32_e64 s[62:63], v65, v175
	v_cmp_ge_f32_e64 s[88:89], v59, v175
	v_cmp_ge_f32_e64 s[6:7], v56, v175
	v_cmp_ge_f32_e64 s[8:9], v53, v176
	v_cmp_ge_f32_e64 s[2:3], v52, v176
	v_cmp_ge_f32_e64 s[80:81], v50, v176
	s_bcnt1_i32_b64 s13, s[90:91]
	s_bcnt1_i32_b64 s1, s[92:93]
	s_add_u32 s13, s13, s1
	s_bcnt1_i32_b64 s1, s[94:95]
	s_add_u32 s13, s13, s1
	s_bcnt1_i32_b64 s1, s[96:97]
	s_add_u32 s13, s13, s1
	s_bcnt1_i32_b64 s1, s[98:99]
	s_add_u32 s13, s13, s1
	s_bcnt1_i32_b64 s1, s[60:61]
	s_add_u32 s13, s13, s1
	s_bcnt1_i32_b64 s1, s[62:63]
	s_add_u32 s13, s13, s1
	s_bcnt1_i32_b64 s1, s[88:89]
	s_add_u32 s13, s13, s1
	s_bcnt1_i32_b64 s1, s[6:7]
	s_add_u32 s13, s13, s1
	s_bcnt1_i32_b64 s1, s[8:9]
	s_add_u32 s13, s13, s1
	s_bcnt1_i32_b64 s1, s[2:3]
	s_add_u32 s13, s13, s1
	s_bcnt1_i32_b64 s1, s[80:81]
	s_add_u32 s13, s13, s1
	s_cmp_eq_u32 s13, 0
	s_cbranch_scc1 .Lmy_list_done
	v_mov_b32_e32 v177, 0x13d90
	v_mov_b32_e32 v178, s13
	s_mov_b64 exec, 1
	ds_add_rtn_u32 v179, v177, v178
	s_mov_b64 exec, -1
	s_waitcnt lgkmcnt(0)
	v_readfirstlane_b32 s0, v179
	s_and_saveexec_b64 s[82:83], s[90:91]
	s_cbranch_execz .Lmy_list_skip0
	v_mbcnt_lo_u32_b32 v180, s90, 0
	v_mbcnt_hi_u32_b32 v180, s91, v180
	v_add_u32_e32 v181, 0x0, v60
	v_or_b32_e32 v181, v181, v193
	v_add_lshl_u32 v180, v180, s0, 1
	ds_write_b16 v180, v181
	s_bcnt1_i32_b64 s1, s[90:91]
	s_add_u32 s0, s0, s1
.Lmy_list_skip0:
	s_or_b64 exec, exec, s[82:83]
	s_and_saveexec_b64 s[82:83], s[92:93]
	s_cbranch_execz .Lmy_list_skip1
	v_mbcnt_lo_u32_b32 v180, s92, 0
	v_mbcnt_hi_u32_b32 v180, s93, v180
	v_add_u32_e32 v181, 0x0, v60
	v_or_b32_e32 v181, v181, v194
	v_add_lshl_u32 v180, v180, s0, 1
	ds_write_b16 v180, v181
	s_bcnt1_i32_b64 s1, s[92:93]
	s_add_u32 s0, s0, s1
.Lmy_list_skip1:
	s_or_b64 exec, exec, s[82:83]
	s_and_saveexec_b64 s[82:83], s[94:95]
	s_cbranch_execz .Lmy_list_skip2
	v_mbcnt_lo_u32_b32 v180, s94, 0
	v_mbcnt_hi_u32_b32 v180, s95, v180
	v_add_u32_e32 v181, 0x0, v60
	v_or_b32_e32 v181, v181, v195
	v_add_lshl_u32 v180, v180, s0, 1
	ds_write_b16 v180, v181
	s_bcnt1_i32_b64 s1, s[94:95]
	s_add_u32 s0, s0, s1
.Lmy_list_skip2:
	s_or_b64 exec, exec, s[82:83]
	s_and_saveexec_b64 s[82:83], s[96:97]
	s_cbranch_execz .Lmy_list_skip3
	v_mbcnt_lo_u32_b32 v180, s96, 0
	v_mbcnt_hi_u32_b32 v180, s97, v180
	v_add_u32_e32 v181, 0x100, v60
	v_or_b32_e32 v181, v181, v193
	v_add_lshl_u32 v180, v180, s0, 1
	ds_write_b16 v180, v181
	s_bcnt1_i32_b64 s1, s[96:97]
	s_add_u32 s0, s0, s1
.Lmy_list_skip3:
	s_or_b64 exec, exec, s[82:83]
	s_and_saveexec_b64 s[82:83], s[98:99]
	s_cbranch_execz .Lmy_list_skip4
	v_mbcnt_lo_u32_b32 v180, s98, 0
	v_mbcnt_hi_u32_b32 v180, s99, v180
	v_add_u32_e32 v181, 0x100, v60
	v_or_b32_e32 v181, v181, v194
	v_add_lshl_u32 v180, v180, s0, 1
	ds_write_b16 v180, v181
	s_bcnt1_i32_b64 s1, s[98:99]
	s_add_u32 s0, s0, s1
.Lmy_list_skip4:
	s_or_b64 exec, exec, s[82:83]
	s_and_saveexec_b64 s[82:83], s[60:61]
	s_cbranch_execz .Lmy_list_skip5
	v_mbcnt_lo_u32_b32 v180, s60, 0
	v_mbcnt_hi_u32_b32 v180, s61, v180
	v_add_u32_e32 v181, 0x100, v60
	v_or_b32_e32 v181, v181, v195
	v_add_lshl_u32 v180, v180, s0, 1
	ds_write_b16 v180, v181
	s_bcnt1_i32_b64 s1, s[60:61]
	s_add_u32 s0, s0, s1
.Lmy_list_skip5:
	s_or_b64 exec, exec, s[82:83]
	s_and_saveexec_b64 s[82:83], s[62:63]
	s_cbranch_execz .Lmy_list_skip6
	v_mbcnt_lo_u32_b32 v180, s62, 0
	v_mbcnt_hi_u32_b32 v180, s63, v180
	v_add_u32_e32 v181, 0x200, v60
	v_or_b32_e32 v181, v181, v193
	v_add_lshl_u32 v180, v180, s0, 1
	ds_write_b16 v180, v181
	s_bcnt1_i32_b64 s1, s[62:63]
	s_add_u32 s0, s0, s1
.Lmy_list_skip6:
	s_or_b64 exec, exec, s[82:83]
	s_and_saveexec_b64 s[82:83], s[88:89]
	s_cbranch_execz .Lmy_list_skip7
	v_mbcnt_lo_u32_b32 v180, s88, 0
	v_mbcnt_hi_u32_b32 v180, s89, v180
	v_add_u32_e32 v181, 0x200, v60
	v_or_b32_e32 v181, v181, v194
	v_add_lshl_u32 v180, v180, s0, 1
	ds_write_b16 v180, v181
	s_bcnt1_i32_b64 s1, s[88:89]
	s_add_u32 s0, s0, s1
.Lmy_list_skip7:
	s_or_b64 exec, exec, s[82:83]
	s_and_saveexec_b64 s[82:83], s[6:7]
	s_cbranch_execz .Lmy_list_skip8
	v_mbcnt_lo_u32_b32 v180, s6, 0
	v_mbcnt_hi_u32_b32 v180, s7, v180
	v_add_u32_e32 v181, 0x200, v60
	v_or_b32_e32 v181, v181, v195
	v_add_lshl_u32 v180, v180, s0, 1
	ds_write_b16 v180, v181
	s_bcnt1_i32_b64 s1, s[6:7]
	s_add_u32 s0, s0, s1
.Lmy_list_skip8:
	s_or_b64 exec, exec, s[82:83]
	s_and_saveexec_b64 s[82:83], s[8:9]
	s_cbranch_execz .Lmy_list_skip9
	v_mbcnt_lo_u32_b32 v180, s8, 0
	v_mbcnt_hi_u32_b32 v180, s9, v180
	v_add_u32_e32 v181, 0x300, v60
	v_or_b32_e32 v181, v181, v193
	v_add_lshl_u32 v180, v180, s0, 1
	ds_write_b16 v180, v181
	s_bcnt1_i32_b64 s1, s[8:9]
	s_add_u32 s0, s0, s1
.Lmy_list_skip9:
	s_or_b64 exec, exec, s[82:83]
	s_and_saveexec_b64 s[82:83], s[2:3]
	s_cbranch_execz .Lmy_list_skip10
	v_mbcnt_lo_u32_b32 v180, s2, 0
	v_mbcnt_hi_u32_b32 v180, s3, v180
	v_add_u32_e32 v181, 0x300, v60
	v_or_b32_e32 v181, v181, v194
	v_add_lshl_u32 v180, v180, s0, 1
	ds_write_b16 v180, v181
	s_bcnt1_i32_b64 s1, s[2:3]
	s_add_u32 s0, s0, s1
.Lmy_list_skip10:
	s_or_b64 exec, exec, s[82:83]
	s_and_saveexec_b64 s[82:83], s[80:81]
	s_cbranch_execz .Lmy_list_skip11
	v_mbcnt_lo_u32_b32 v180, s80, 0
	v_mbcnt_hi_u32_b32 v180, s81, v180
	v_add_u32_e32 v181, 0x300, v60
	v_or_b32_e32 v181, v181, v195
	v_add_lshl_u32 v180, v180, s0, 1
	ds_write_b16 v180, v181
	s_bcnt1_i32_b64 s1, s[80:81]
	s_add_u32 s0, s0, s1

	.amdhsa_kernel _Z7k_fine3PKfS0_PKtS2_PKdS4_S0_PiPfS5_S0_S0_PtS7_
		.amdhsa_group_segment_fixed_size 0
		.amdhsa_private_segment_fixed_size 0
		.amdhsa_kernarg_size 112
		.amdhsa_user_sgpr_count 2
		.amdhsa_user_sgpr_dispatch_ptr 0
		.amdhsa_user_sgpr_queue_ptr 0
		.amdhsa_user_sgpr_kernarg_segment_ptr 1
		.amdhsa_user_sgpr_dispatch_id 0
		.amdhsa_user_sgpr_kernarg_preload_length 0
		.amdhsa_user_sgpr_kernarg_preload_offset 0
		.amdhsa_user_sgpr_private_segment_size 0
		.amdhsa_uses_dynamic_stack 0
		.amdhsa_enable_private_segment 0
		.amdhsa_system_sgpr_workgroup_id_x 1
		.amdhsa_system_sgpr_workgroup_id_y 0
		.amdhsa_system_sgpr_workgroup_id_z 0
		.amdhsa_system_sgpr_workgroup_info 0
		.amdhsa_system_vgpr_workitem_id 0
		.amdhsa_next_free_vgpr 234
		.amdhsa_next_free_sgpr 100
		.amdhsa_accum_offset 236
		.amdhsa_reserve_vcc 1
		.amdhsa_float_round_mode_32 0
		.amdhsa_float_round_mode_16_64 0
		.amdhsa_float_denorm_mode_32 3
		.amdhsa_float_denorm_mode_16_64 3
		.amdhsa_dx10_clamp 1
		.amdhsa_ieee_mode 1
		.amdhsa_fp16_overflow 0
		.amdhsa_tg_split 0
		.amdhsa_exception_fp_ieee_invalid_op 0
		.amdhsa_exception_fp_denorm_src 0
		.amdhsa_exception_fp_ieee_div_zero 0
		.amdhsa_exception_fp_ieee_overflow 0
		.amdhsa_exception_fp_ieee_underflow 0
		.amdhsa_exception_fp_ieee_inexact 0
		.amdhsa_exception_int_div_zero 0
	.end_amdhsa_kernel

amdhsa.kernels:
  - .agpr_count:     0
    .args:
      - .actual_access:  read_only
        .address_space:  global
        .offset:         0
        .size:           8
        .value_kind:     global_buffer
      - .actual_access:  read_only
        .address_space:  global
        .offset:         8
        .size:           8
        .value_kind:     global_buffer
      - .actual_access:  write_only
        .address_space:  global
        .offset:         16
        .size:           8
        .value_kind:     global_buffer
      - .actual_access:  write_only
        .address_space:  global
        .offset:         24
        .size:           8
        .value_kind:     global_buffer
      - .actual_access:  write_only
        .address_space:  global
        .offset:         32
        .size:           8
        .value_kind:     global_buffer
      - .actual_access:  write_only
        .address_space:  global
        .offset:         40
        .size:           8
        .value_kind:     global_buffer
      - .actual_access:  write_only
        .address_space:  global
        .offset:         48
        .size:           8
        .value_kind:     global_buffer
      - .actual_access:  write_only
        .address_space:  global
        .offset:         56
        .size:           8
        .value_kind:     global_buffer
      - .actual_access:  write_only
        .address_space:  global
        .offset:         64
        .size:           8
        .value_kind:     global_buffer
    .group_segment_fixed_size: 18944
    .kernarg_segment_align: 8
    .kernarg_segment_size: 72
    .language:       OpenCL C
    .language_version:
      - 2
      - 0
    .max_flat_workgroup_size: 256
    .name:           _Z6k_prepPKfS0_PfS1_PdS2_PtS3_S3_
    .private_segment_fixed_size: 0
    .sgpr_count:     34
    .sgpr_spill_count: 0
    .symbol:         _Z6k_prepPKfS0_PfS1_PdS2_PtS3_S3_.kd
    .uniform_work_group_size: 1
    .uses_dynamic_stack: false
    .vgpr_count:     29
    .vgpr_spill_count: 0
    .wavefront_size: 64
  - .agpr_count:     16
    .args:
      - .actual_access:  read_only
        .address_space:  global
        .offset:         0
        .size:           8
        .value_kind:     global_buffer
      - .actual_access:  read_only
        .address_space:  global
        .offset:         8
        .size:           8
        .value_kind:     global_buffer
      - .actual_access:  read_only
        .address_space:  global
        .offset:         16
        .size:           8
        .value_kind:     global_buffer
      - .actual_access:  read_only
        .address_space:  global
        .offset:         24
        .size:           8
        .value_kind:     global_buffer
      - .actual_access:  write_only
        .address_space:  global
        .offset:         32
        .size:           8
        .value_kind:     global_buffer
    .group_segment_fixed_size: 256
    .kernarg_segment_align: 8
    .kernarg_segment_size: 40
    .language:       OpenCL C
    .language_version:
      - 2
      - 0
    .max_flat_workgroup_size: 256
    .name:           _Z9k_coarse2PKtS0_PKdS2_Pf
    .private_segment_fixed_size: 0
    .sgpr_count:     37
    .sgpr_spill_count: 0
    .symbol:         _Z9k_coarse2PKtS0_PKdS2_Pf.kd
    .uniform_work_group_size: 1
    .uses_dynamic_stack: false
    .vgpr_count:     156
    .vgpr_spill_count: 0
    .wavefront_size: 64
  - .agpr_count:     0
    .args:
      - .actual_access:  read_only
        .address_space:  global
        .offset:         0
        .size:           8
        .value_kind:     global_buffer
      - .actual_access:  read_only
        .address_space:  global
        .offset:         8
        .size:           8
        .value_kind:     global_buffer
      - .actual_access:  read_only
        .address_space:  global
        .offset:         16
        .size:           8
        .value_kind:     global_buffer
      - .actual_access:  read_only
        .address_space:  global
        .offset:         24
        .size:           8
        .value_kind:     global_buffer
      - .actual_access:  read_only
        .address_space:  global
        .offset:         32
        .size:           8
        .value_kind:     global_buffer
      - .actual_access:  read_only
        .address_space:  global
        .offset:         40
        .size:           8
        .value_kind:     global_buffer
      - .actual_access:  read_only
        .address_space:  global
        .offset:         48
        .size:           8
        .value_kind:     global_buffer
      - .actual_access:  write_only
        .address_space:  global
        .offset:         56
        .size:           8
        .value_kind:     global_buffer
      - .actual_access:  write_only
        .address_space:  global
        .offset:         64
        .size:           8
        .value_kind:     global_buffer
      - .actual_access:  write_only
        .address_space:  global
        .offset:         72
        .size:           8
        .value_kind:     global_buffer
      - .actual_access:  read_only
        .address_space:  global
        .offset:         80
        .size:           8
        .value_kind:     global_buffer
      - .actual_access:  read_only
        .address_space:  global
        .offset:         88
        .size:           8
        .value_kind:     global_buffer
      - .actual_access:  write_only
        .address_space:  global
        .offset:         96
        .size:           8
        .value_kind:     global_buffer
      - .actual_access:  write_only
        .address_space:  global
        .offset:         104
        .size:           8
        .value_kind:     global_buffer
    .group_segment_fixed_size: 0
    .kernarg_segment_align: 8
    .kernarg_segment_size: 112
    .language:       OpenCL C
    .language_version:
      - 2
      - 0
    .max_flat_workgroup_size: 512
    .name:           _Z7k_fine3PKfS0_PKtS2_PKdS4_S0_PiPfS5_S0_S0_PtS7_
    .private_segment_fixed_size: 0
    .sgpr_count:     106
    .sgpr_spill_count: 4
    .symbol:         _Z7k_fine3PKfS0_PKtS2_PKdS4_S0_PiPfS5_S0_S0_PtS7_.kd
    .uniform_work_group_size: 1
    .uses_dynamic_stack: false
    .vgpr_count:     234
    .vgpr_spill_count: 0
    .wavefront_size: 64
  - .agpr_count:     0
    .args:
      - .actual_access:  read_only
        .address_space:  global
        .offset:         0
        .size:           8
        .value_kind:     global_buffer
      - .actual_access:  read_only
        .address_space:  global
        .offset:         8
        .size:           8
        .value_kind:     global_buffer
      - .actual_access:  read_only
        .address_space:  global
        .offset:         16
        .size:           8
        .value_kind:     global_buffer
      - .actual_access:  read_only
        .address_space:  global
        .offset:         24
        .size:           8
        .value_kind:     global_buffer
      - .actual_access:  read_only
        .address_space:  global
        .offset:         32
        .size:           8
        .value_kind:     global_buffer
      - .actual_access:  read_only
        .address_space:  global
        .offset:         40
        .size:           8
        .value_kind:     global_buffer
      - .actual_access:  write_only
        .address_space:  global
        .offset:         48
        .size:           8
        .value_kind:     global_buffer
      - .actual_access:  write_only
        .address_space:  global
        .offset:         56
        .size:           8
        .value_kind:     global_buffer
      - .actual_access:  write_only
        .address_space:  global
        .offset:         64
        .size:           8
        .value_kind:     global_buffer
    .group_segment_fixed_size: 18512
    .kernarg_segment_align: 8
    .kernarg_segment_size: 72
    .language:       OpenCL C
    .language_version:
      - 2
      - 0
    .max_flat_workgroup_size: 256
    .name:           _Z10k_transferPKtS0_PKfPKiS2_S4_PfS5_S5_
    .private_segment_fixed_size: 0
    .sgpr_count:     34
    .sgpr_spill_count: 0
    .symbol:         _Z10k_transferPKtS0_PKfPKiS2_S4_PfS5_S5_.kd
    .uniform_work_group_size: 1
    .uses_dynamic_stack: false
    .vgpr_count:     49
    .vgpr_spill_count: 0
    .wavefront_size: 64
